# baseline (speedup 1.0000x reference)
.Lu0_2:
	s_waitcnt lgkmcnt(14)
	v_mfma_f32_32x32x16_f16 v[2:17], v[158:161], v[178:181], v[2:17]
	v_exp_f32_e32 v98, v98
	v_exp_f32_e32 v99, v99
	v_exp_f32_e32 v100, v100
	v_exp_f32_e32 v101, v101
	s_waitcnt lgkmcnt(12)
	v_mfma_f32_32x32x16_f16 v[18:33], v[158:161], v[174:177], v[18:33]
	v_exp_f32_e32 v102, v102
	ds_read_b128 v[58:61], v211 offset:16384
	v_exp_f32_e32 v103, v103
	ds_read_b128 v[114:117], v211 offset:20480
	v_exp_f32_e32 v104, v104
	v_exp_f32_e32 v105, v105
	s_waitcnt lgkmcnt(12)
	v_mfma_f32_32x32x16_f16 v[2:17], v[150:153], v[170:173], v[2:17]
	v_exp_f32_e32 v106, v106
	ds_read_b128 v[182:185], v210 offset:16384
	v_exp_f32_e32 v107, v107
	ds_read_b128 v[174:177], v210 offset:20480
	v_exp_f32_e32 v108, v108
	v_exp_f32_e32 v109, v109
	s_waitcnt lgkmcnt(12)
	v_mfma_f32_32x32x16_f16 v[18:33], v[150:153], v[74:77], v[18:33]
	v_exp_f32_e32 v110, v110
	ds_read_b128 v[178:181], v209 offset:16384
	v_exp_f32_e32 v111, v111
	ds_read_b128 v[166:169], v209 offset:20480
	v_exp_f32_e32 v112, v112
	v_exp_f32_e32 v113, v113
	s_waitcnt lgkmcnt(12)
	v_mfma_f32_32x32x16_f16 v[2:17], v[142:145], v[70:73], v[2:17]
	v_exp_f32_e32 v82, v82
	ds_read_b128 v[170:173], v208 offset:16384
	v_exp_f32_e32 v83, v83
	ds_read_b128 v[162:165], v208 offset:20480
	v_exp_f32_e32 v84, v84
	v_exp_f32_e32 v85, v85
	s_waitcnt lgkmcnt(12)
	v_mfma_f32_32x32x16_f16 v[18:33], v[142:145], v[66:69], v[18:33]
	v_exp_f32_e32 v86, v86
	v_exp_f32_e32 v87, v87
	v_exp_f32_e32 v88, v88
	v_exp_f32_e32 v89, v89
	s_waitcnt lgkmcnt(10)
	v_mfma_f32_32x32x16_f16 v[2:17], v[130:133], v[54:57], v[2:17]
	v_exp_f32_e32 v90, v90
	v_exp_f32_e32 v91, v91
	v_exp_f32_e32 v92, v92
	v_exp_f32_e32 v93, v93
	s_waitcnt lgkmcnt(8)
	v_mfma_f32_32x32x16_f16 v[18:33], v[130:133], v[50:53], v[18:33]
	v_exp_f32_e32 v94, v94
	v_exp_f32_e32 v95, v95
	v_exp_f32_e32 v96, v96
	v_exp_f32_e32 v97, v97
	s_waitcnt vmcnt(2) lgkmcnt(0)
	s_barrier
	s_andn2_b64 vcc, exec, s[26:27]
	s_cbranch_vccnz .Lu0_4
	s_waitcnt lgkmcnt(0)
	v_add_u32_e32 v66, s38, v212
	ds_read_b128 v[50:53], v66 offset:49248
	ds_read_b128 v[54:57], v66 offset:49216
	ds_read_b128 v[62:65], v66 offset:49184
	ds_read_b128 v[66:69], v66 offset:49152
	s_waitcnt lgkmcnt(3)
	v_pk_mul_f32 v[14:15], v[14:15], v[50:51]
	s_waitcnt lgkmcnt(2)
	v_pk_mul_f32 v[10:11], v[10:11], v[54:55]
	s_waitcnt lgkmcnt(1)
	v_pk_mul_f32 v[6:7], v[6:7], v[62:63]
	v_pk_mul_f32 v[16:17], v[16:17], v[52:53]
	v_pk_mul_f32 v[12:13], v[12:13], v[56:57]
	v_pk_mul_f32 v[8:9], v[8:9], v[64:65]
	s_waitcnt lgkmcnt(0)
	v_pk_mul_f32 v[4:5], v[4:5], v[68:69]
	v_pk_mul_f32 v[2:3], v[2:3], v[66:67]
	v_pk_mul_f32 v[30:31], v[30:31], v[50:51]
	v_pk_mul_f32 v[26:27], v[26:27], v[54:55]
	v_pk_mul_f32 v[22:23], v[22:23], v[62:63]
	v_pk_mul_f32 v[32:33], v[32:33], v[52:53]
	v_pk_mul_f32 v[28:29], v[28:29], v[56:57]
	v_pk_mul_f32 v[24:25], v[24:25], v[64:65]
	v_pk_mul_f32 v[20:21], v[20:21], v[68:69]
	v_pk_mul_f32 v[18:19], v[18:19], v[66:67]

.Lu0_5:
	s_waitcnt lgkmcnt(14)
	v_mfma_f32_32x32x16_f16 v[2:17], v[158:161], v[126:129], v[2:17]
	v_exp_f32_e32 v66, v66
	v_exp_f32_e32 v67, v67
	v_exp_f32_e32 v68, v68
	v_exp_f32_e32 v69, v69
	s_waitcnt lgkmcnt(12)
	v_mfma_f32_32x32x16_f16 v[18:33], v[158:161], v[122:125], v[18:33]
	v_exp_f32_e32 v70, v70
	ds_read_b128 v[82:85], v211
	v_exp_f32_e32 v71, v71
	ds_read_b128 v[170:173], v211 offset:4096
	v_exp_f32_e32 v72, v72
	v_exp_f32_e32 v73, v73
	s_waitcnt lgkmcnt(12)
	v_mfma_f32_32x32x16_f16 v[2:17], v[150:153], v[118:121], v[2:17]
	v_exp_f32_e32 v74, v74
	ds_read_b128 v[166:169], v210
	v_exp_f32_e32 v75, v75
	ds_read_b128 v[162:165], v210 offset:4096
	v_exp_f32_e32 v76, v76
	v_exp_f32_e32 v77, v77
	s_waitcnt lgkmcnt(12)
	v_mfma_f32_32x32x16_f16 v[18:33], v[150:153], v[114:117], v[18:33]
	v_exp_f32_e32 v78, v78
	ds_read_b128 v[126:129], v209
	v_exp_f32_e32 v79, v79
	ds_read_b128 v[122:125], v209 offset:4096
	v_exp_f32_e32 v80, v80
	v_exp_f32_e32 v81, v81
	s_waitcnt lgkmcnt(12)
	v_mfma_f32_32x32x16_f16 v[2:17], v[142:145], v[106:109], v[2:17]
	v_exp_f32_e32 v50, v50
	ds_read_b128 v[118:121], v208
	v_exp_f32_e32 v51, v51
	ds_read_b128 v[114:117], v208 offset:4096
	v_exp_f32_e32 v52, v52
	v_exp_f32_e32 v53, v53
	s_waitcnt lgkmcnt(12)
	v_mfma_f32_32x32x16_f16 v[18:33], v[142:145], v[102:105], v[18:33]
	v_exp_f32_e32 v54, v54
	v_exp_f32_e32 v55, v55
	v_exp_f32_e32 v56, v56
	v_exp_f32_e32 v57, v57
	s_waitcnt lgkmcnt(10)
	v_mfma_f32_32x32x16_f16 v[2:17], v[130:133], v[98:101], v[2:17]
	v_exp_f32_e32 v58, v58
	v_exp_f32_e32 v59, v59
	v_exp_f32_e32 v60, v60
	v_exp_f32_e32 v61, v61
	s_waitcnt lgkmcnt(8)
	v_mfma_f32_32x32x16_f16 v[18:33], v[130:133], v[86:89], v[18:33]
	v_exp_f32_e32 v62, v62
	v_exp_f32_e32 v63, v63
	v_exp_f32_e32 v64, v64
	v_exp_f32_e32 v65, v65
	s_waitcnt vmcnt(2) lgkmcnt(0)
	s_barrier
	s_andn2_b64 vcc, exec, s[26:27]
	s_cbranch_vccnz .Lu0_7
	s_waitcnt lgkmcnt(0)
	v_add_u32_e32 v98, s38, v212
	ds_read_b128 v[86:89], v98 offset:49248
	ds_read_b128 v[90:93], v98 offset:49216
	ds_read_b128 v[94:97], v98 offset:49152
	ds_read_b128 v[98:101], v98 offset:49184
	s_waitcnt lgkmcnt(3)
	v_pk_mul_f32 v[16:17], v[16:17], v[88:89]
	v_pk_mul_f32 v[14:15], v[14:15], v[86:87]
	s_waitcnt lgkmcnt(2)
	v_pk_mul_f32 v[12:13], v[12:13], v[92:93]
	v_pk_mul_f32 v[10:11], v[10:11], v[90:91]
	s_waitcnt lgkmcnt(0)
	v_pk_mul_f32 v[8:9], v[8:9], v[100:101]
	v_pk_mul_f32 v[6:7], v[6:7], v[98:99]
	v_pk_mul_f32 v[4:5], v[4:5], v[96:97]
	v_pk_mul_f32 v[2:3], v[2:3], v[94:95]
	v_pk_mul_f32 v[32:33], v[32:33], v[88:89]
	v_pk_mul_f32 v[30:31], v[30:31], v[86:87]
	v_pk_mul_f32 v[28:29], v[28:29], v[92:93]
	v_pk_mul_f32 v[26:27], v[26:27], v[90:91]
	v_pk_mul_f32 v[24:25], v[24:25], v[100:101]
	v_pk_mul_f32 v[22:23], v[22:23], v[98:99]
	v_pk_mul_f32 v[20:21], v[20:21], v[96:97]
	v_pk_mul_f32 v[18:19], v[18:19], v[94:95]

.Lu1_2:
	s_waitcnt lgkmcnt(14)
	v_mfma_f32_32x32x16_f16 v[2:17], v[158:161], v[178:181], v[2:17]
	v_exp_f32_e32 v98, v98
	v_exp_f32_e32 v99, v99
	v_exp_f32_e32 v100, v100
	v_exp_f32_e32 v101, v101
	s_waitcnt lgkmcnt(12)
	v_mfma_f32_32x32x16_f16 v[18:33], v[158:161], v[174:177], v[18:33]
	v_exp_f32_e32 v102, v102
	ds_read_b128 v[58:61], v211 offset:8192
	v_exp_f32_e32 v103, v103
	ds_read_b128 v[114:117], v211 offset:12288
	v_exp_f32_e32 v104, v104
	v_exp_f32_e32 v105, v105
	s_waitcnt lgkmcnt(12)
	v_mfma_f32_32x32x16_f16 v[2:17], v[150:153], v[170:173], v[2:17]
	v_exp_f32_e32 v106, v106
	ds_read_b128 v[182:185], v210 offset:8192
	v_exp_f32_e32 v107, v107
	ds_read_b128 v[174:177], v210 offset:12288
	v_exp_f32_e32 v108, v108
	v_exp_f32_e32 v109, v109
	s_waitcnt lgkmcnt(12)
	v_mfma_f32_32x32x16_f16 v[18:33], v[150:153], v[74:77], v[18:33]
	v_exp_f32_e32 v110, v110
	ds_read_b128 v[178:181], v209 offset:8192
	v_exp_f32_e32 v111, v111
	ds_read_b128 v[166:169], v209 offset:12288
	v_exp_f32_e32 v112, v112
	v_exp_f32_e32 v113, v113
	s_waitcnt lgkmcnt(12)
	v_mfma_f32_32x32x16_f16 v[2:17], v[142:145], v[70:73], v[2:17]
	v_exp_f32_e32 v82, v82
	ds_read_b128 v[170:173], v208 offset:8192
	v_exp_f32_e32 v83, v83
	ds_read_b128 v[162:165], v208 offset:12288
	v_exp_f32_e32 v84, v84
	v_exp_f32_e32 v85, v85
	s_waitcnt lgkmcnt(12)
	v_mfma_f32_32x32x16_f16 v[18:33], v[142:145], v[66:69], v[18:33]
	v_exp_f32_e32 v86, v86
	v_exp_f32_e32 v87, v87
	v_exp_f32_e32 v88, v88
	v_exp_f32_e32 v89, v89
	s_waitcnt lgkmcnt(10)
	v_mfma_f32_32x32x16_f16 v[2:17], v[130:133], v[54:57], v[2:17]
	v_exp_f32_e32 v90, v90
	v_exp_f32_e32 v91, v91
	v_exp_f32_e32 v92, v92
	v_exp_f32_e32 v93, v93
	s_waitcnt lgkmcnt(8)
	v_mfma_f32_32x32x16_f16 v[18:33], v[130:133], v[50:53], v[18:33]
	v_exp_f32_e32 v94, v94
	v_exp_f32_e32 v95, v95
	v_exp_f32_e32 v96, v96
	v_exp_f32_e32 v97, v97
	s_waitcnt vmcnt(2) lgkmcnt(0)
	s_barrier
	s_andn2_b64 vcc, exec, s[26:27]
	s_cbranch_vccnz .Lu1_4
	s_waitcnt lgkmcnt(0)
	v_add_u32_e32 v66, s38, v212
	ds_read_b128 v[50:53], v66 offset:49248
	ds_read_b128 v[54:57], v66 offset:49216
	ds_read_b128 v[62:65], v66 offset:49184
	ds_read_b128 v[66:69], v66 offset:49152
	s_waitcnt lgkmcnt(3)
	v_pk_mul_f32 v[14:15], v[14:15], v[50:51]
	s_waitcnt lgkmcnt(2)
	v_pk_mul_f32 v[10:11], v[10:11], v[54:55]
	s_waitcnt lgkmcnt(1)
	v_pk_mul_f32 v[6:7], v[6:7], v[62:63]
	v_pk_mul_f32 v[16:17], v[16:17], v[52:53]
	v_pk_mul_f32 v[12:13], v[12:13], v[56:57]
	v_pk_mul_f32 v[8:9], v[8:9], v[64:65]
	s_waitcnt lgkmcnt(0)
	v_pk_mul_f32 v[4:5], v[4:5], v[68:69]
	v_pk_mul_f32 v[2:3], v[2:3], v[66:67]
	v_pk_mul_f32 v[30:31], v[30:31], v[50:51]
	v_pk_mul_f32 v[26:27], v[26:27], v[54:55]
	v_pk_mul_f32 v[22:23], v[22:23], v[62:63]
	v_pk_mul_f32 v[32:33], v[32:33], v[52:53]
	v_pk_mul_f32 v[28:29], v[28:29], v[56:57]
	v_pk_mul_f32 v[24:25], v[24:25], v[64:65]
	v_pk_mul_f32 v[20:21], v[20:21], v[68:69]
	v_pk_mul_f32 v[18:19], v[18:19], v[66:67]

.Lu1_5:
	s_waitcnt lgkmcnt(14)
	v_mfma_f32_32x32x16_f16 v[2:17], v[158:161], v[126:129], v[2:17]
	v_exp_f32_e32 v66, v66
	v_exp_f32_e32 v67, v67
	v_exp_f32_e32 v68, v68
	v_exp_f32_e32 v69, v69
	s_waitcnt lgkmcnt(12)
	v_mfma_f32_32x32x16_f16 v[18:33], v[158:161], v[122:125], v[18:33]
	v_exp_f32_e32 v70, v70
	ds_read_b128 v[82:85], v211 offset:16384
	v_exp_f32_e32 v71, v71
	ds_read_b128 v[170:173], v211 offset:20480
	v_exp_f32_e32 v72, v72
	v_exp_f32_e32 v73, v73
	s_waitcnt lgkmcnt(12)
	v_mfma_f32_32x32x16_f16 v[2:17], v[150:153], v[118:121], v[2:17]
	v_exp_f32_e32 v74, v74
	ds_read_b128 v[166:169], v210 offset:16384
	v_exp_f32_e32 v75, v75
	ds_read_b128 v[162:165], v210 offset:20480
	v_exp_f32_e32 v76, v76
	v_exp_f32_e32 v77, v77
	s_waitcnt lgkmcnt(12)
	v_mfma_f32_32x32x16_f16 v[18:33], v[150:153], v[114:117], v[18:33]
	v_exp_f32_e32 v78, v78
	ds_read_b128 v[126:129], v209 offset:16384
	v_exp_f32_e32 v79, v79
	ds_read_b128 v[122:125], v209 offset:20480
	v_exp_f32_e32 v80, v80
	v_exp_f32_e32 v81, v81
	s_waitcnt lgkmcnt(12)
	v_mfma_f32_32x32x16_f16 v[2:17], v[142:145], v[106:109], v[2:17]
	v_exp_f32_e32 v50, v50
	ds_read_b128 v[118:121], v208 offset:16384
	v_exp_f32_e32 v51, v51
	ds_read_b128 v[114:117], v208 offset:20480
	v_exp_f32_e32 v52, v52
	v_exp_f32_e32 v53, v53
	s_waitcnt lgkmcnt(12)
	v_mfma_f32_32x32x16_f16 v[18:33], v[142:145], v[102:105], v[18:33]
	v_exp_f32_e32 v54, v54
	v_exp_f32_e32 v55, v55
	v_exp_f32_e32 v56, v56
	v_exp_f32_e32 v57, v57
	s_waitcnt lgkmcnt(10)
	v_mfma_f32_32x32x16_f16 v[2:17], v[130:133], v[98:101], v[2:17]
	v_exp_f32_e32 v58, v58
	v_exp_f32_e32 v59, v59
	v_exp_f32_e32 v60, v60
	v_exp_f32_e32 v61, v61
	s_waitcnt lgkmcnt(8)
	v_mfma_f32_32x32x16_f16 v[18:33], v[130:133], v[86:89], v[18:33]
	v_exp_f32_e32 v62, v62
	v_exp_f32_e32 v63, v63
	v_exp_f32_e32 v64, v64
	v_exp_f32_e32 v65, v65
	s_waitcnt vmcnt(2) lgkmcnt(0)
	s_barrier
	s_andn2_b64 vcc, exec, s[26:27]
	s_cbranch_vccnz .Lu1_7
	s_waitcnt lgkmcnt(0)
	v_add_u32_e32 v98, s38, v212
	ds_read_b128 v[86:89], v98 offset:49248
	ds_read_b128 v[90:93], v98 offset:49216
	ds_read_b128 v[94:97], v98 offset:49152
	ds_read_b128 v[98:101], v98 offset:49184
	s_waitcnt lgkmcnt(3)
	v_pk_mul_f32 v[16:17], v[16:17], v[88:89]
	v_pk_mul_f32 v[14:15], v[14:15], v[86:87]
	s_waitcnt lgkmcnt(2)
	v_pk_mul_f32 v[12:13], v[12:13], v[92:93]
	v_pk_mul_f32 v[10:11], v[10:11], v[90:91]
	s_waitcnt lgkmcnt(0)
	v_pk_mul_f32 v[8:9], v[8:9], v[100:101]
	v_pk_mul_f32 v[6:7], v[6:7], v[98:99]
	v_pk_mul_f32 v[4:5], v[4:5], v[96:97]
	v_pk_mul_f32 v[2:3], v[2:3], v[94:95]
	v_pk_mul_f32 v[32:33], v[32:33], v[88:89]
	v_pk_mul_f32 v[30:31], v[30:31], v[86:87]
	v_pk_mul_f32 v[28:29], v[28:29], v[92:93]
	v_pk_mul_f32 v[26:27], v[26:27], v[90:91]
	v_pk_mul_f32 v[24:25], v[24:25], v[100:101]
	v_pk_mul_f32 v[22:23], v[22:23], v[98:99]
	v_pk_mul_f32 v[20:21], v[20:21], v[96:97]
	v_pk_mul_f32 v[18:19], v[18:19], v[94:95]

.Lu2_2:
	s_waitcnt lgkmcnt(14)
	v_mfma_f32_32x32x16_f16 v[2:17], v[158:161], v[178:181], v[2:17]
	v_exp_f32_e32 v98, v98
	v_exp_f32_e32 v99, v99
	v_exp_f32_e32 v100, v100
	v_exp_f32_e32 v101, v101
	s_waitcnt lgkmcnt(12)
	v_mfma_f32_32x32x16_f16 v[18:33], v[158:161], v[174:177], v[18:33]
	v_exp_f32_e32 v102, v102
	ds_read_b128 v[58:61], v211
	v_exp_f32_e32 v103, v103
	ds_read_b128 v[114:117], v211 offset:4096
	v_exp_f32_e32 v104, v104
	v_exp_f32_e32 v105, v105
	s_waitcnt lgkmcnt(12)
	v_mfma_f32_32x32x16_f16 v[2:17], v[150:153], v[170:173], v[2:17]
	v_exp_f32_e32 v106, v106
	ds_read_b128 v[182:185], v210
	v_exp_f32_e32 v107, v107
	ds_read_b128 v[174:177], v210 offset:4096
	v_exp_f32_e32 v108, v108
	v_exp_f32_e32 v109, v109
	s_waitcnt lgkmcnt(12)
	v_mfma_f32_32x32x16_f16 v[18:33], v[150:153], v[74:77], v[18:33]
	v_exp_f32_e32 v110, v110
	ds_read_b128 v[178:181], v209
	v_exp_f32_e32 v111, v111
	ds_read_b128 v[166:169], v209 offset:4096
	v_exp_f32_e32 v112, v112
	v_exp_f32_e32 v113, v113
	s_waitcnt lgkmcnt(12)
	v_mfma_f32_32x32x16_f16 v[2:17], v[142:145], v[70:73], v[2:17]
	v_exp_f32_e32 v82, v82
	ds_read_b128 v[170:173], v208
	v_exp_f32_e32 v83, v83
	ds_read_b128 v[162:165], v208 offset:4096
	v_exp_f32_e32 v84, v84
	v_exp_f32_e32 v85, v85
	s_waitcnt lgkmcnt(12)
	v_mfma_f32_32x32x16_f16 v[18:33], v[142:145], v[66:69], v[18:33]
	v_exp_f32_e32 v86, v86
	v_exp_f32_e32 v87, v87
	v_exp_f32_e32 v88, v88
	v_exp_f32_e32 v89, v89
	s_waitcnt lgkmcnt(10)
	v_mfma_f32_32x32x16_f16 v[2:17], v[130:133], v[54:57], v[2:17]
	v_exp_f32_e32 v90, v90
	v_exp_f32_e32 v91, v91
	v_exp_f32_e32 v92, v92
	v_exp_f32_e32 v93, v93
	s_waitcnt lgkmcnt(8)
	v_mfma_f32_32x32x16_f16 v[18:33], v[130:133], v[50:53], v[18:33]
	v_exp_f32_e32 v94, v94
	v_exp_f32_e32 v95, v95
	v_exp_f32_e32 v96, v96
	v_exp_f32_e32 v97, v97
	s_waitcnt vmcnt(2) lgkmcnt(0)
	s_barrier
	s_andn2_b64 vcc, exec, s[26:27]
	s_cbranch_vccnz .Lu2_4
	s_waitcnt lgkmcnt(0)
	v_add_u32_e32 v66, s38, v212
	ds_read_b128 v[50:53], v66 offset:49248
	ds_read_b128 v[54:57], v66 offset:49216
	ds_read_b128 v[62:65], v66 offset:49184
	ds_read_b128 v[66:69], v66 offset:49152
	s_waitcnt lgkmcnt(3)
	v_pk_mul_f32 v[14:15], v[14:15], v[50:51]
	s_waitcnt lgkmcnt(2)
	v_pk_mul_f32 v[10:11], v[10:11], v[54:55]
	s_waitcnt lgkmcnt(1)
	v_pk_mul_f32 v[6:7], v[6:7], v[62:63]
	v_pk_mul_f32 v[16:17], v[16:17], v[52:53]
	v_pk_mul_f32 v[12:13], v[12:13], v[56:57]
	v_pk_mul_f32 v[8:9], v[8:9], v[64:65]
	s_waitcnt lgkmcnt(0)
	v_pk_mul_f32 v[4:5], v[4:5], v[68:69]
	v_pk_mul_f32 v[2:3], v[2:3], v[66:67]
	v_pk_mul_f32 v[30:31], v[30:31], v[50:51]
	v_pk_mul_f32 v[26:27], v[26:27], v[54:55]
	v_pk_mul_f32 v[22:23], v[22:23], v[62:63]
	v_pk_mul_f32 v[32:33], v[32:33], v[52:53]
	v_pk_mul_f32 v[28:29], v[28:29], v[56:57]
	v_pk_mul_f32 v[24:25], v[24:25], v[64:65]
	v_pk_mul_f32 v[20:21], v[20:21], v[68:69]
	v_pk_mul_f32 v[18:19], v[18:19], v[66:67]

.Lu2_5:
	s_waitcnt lgkmcnt(14)
	v_mfma_f32_32x32x16_f16 v[2:17], v[158:161], v[126:129], v[2:17]
	v_exp_f32_e32 v66, v66
	v_exp_f32_e32 v67, v67
	v_exp_f32_e32 v68, v68
	v_exp_f32_e32 v69, v69
	s_waitcnt lgkmcnt(12)
	v_mfma_f32_32x32x16_f16 v[18:33], v[158:161], v[122:125], v[18:33]
	v_exp_f32_e32 v70, v70
	ds_read_b128 v[82:85], v211 offset:8192
	v_exp_f32_e32 v71, v71
	ds_read_b128 v[170:173], v211 offset:12288
	v_exp_f32_e32 v72, v72
	v_exp_f32_e32 v73, v73
	s_waitcnt lgkmcnt(12)
	v_mfma_f32_32x32x16_f16 v[2:17], v[150:153], v[118:121], v[2:17]
	v_exp_f32_e32 v74, v74
	ds_read_b128 v[166:169], v210 offset:8192
	v_exp_f32_e32 v75, v75
	ds_read_b128 v[162:165], v210 offset:12288
	v_exp_f32_e32 v76, v76
	v_exp_f32_e32 v77, v77
	s_waitcnt lgkmcnt(12)
	v_mfma_f32_32x32x16_f16 v[18:33], v[150:153], v[114:117], v[18:33]
	v_exp_f32_e32 v78, v78
	ds_read_b128 v[126:129], v209 offset:8192
	v_exp_f32_e32 v79, v79
	ds_read_b128 v[122:125], v209 offset:12288
	v_exp_f32_e32 v80, v80
	v_exp_f32_e32 v81, v81
	s_waitcnt lgkmcnt(12)
	v_mfma_f32_32x32x16_f16 v[2:17], v[142:145], v[106:109], v[2:17]
	v_exp_f32_e32 v50, v50
	ds_read_b128 v[118:121], v208 offset:8192
	v_exp_f32_e32 v51, v51
	ds_read_b128 v[114:117], v208 offset:12288
	v_exp_f32_e32 v52, v52
	v_exp_f32_e32 v53, v53
	s_waitcnt lgkmcnt(12)
	v_mfma_f32_32x32x16_f16 v[18:33], v[142:145], v[102:105], v[18:33]
	v_exp_f32_e32 v54, v54
	v_exp_f32_e32 v55, v55
	v_exp_f32_e32 v56, v56
	v_exp_f32_e32 v57, v57
	s_waitcnt lgkmcnt(10)
	v_mfma_f32_32x32x16_f16 v[2:17], v[130:133], v[98:101], v[2:17]
	v_exp_f32_e32 v58, v58
	v_exp_f32_e32 v59, v59
	v_exp_f32_e32 v60, v60
	v_exp_f32_e32 v61, v61
	s_waitcnt lgkmcnt(8)
	v_mfma_f32_32x32x16_f16 v[18:33], v[130:133], v[86:89], v[18:33]
	v_exp_f32_e32 v62, v62
	v_exp_f32_e32 v63, v63
	v_exp_f32_e32 v64, v64
	v_exp_f32_e32 v65, v65
	s_waitcnt vmcnt(2) lgkmcnt(0)
	s_barrier
	s_andn2_b64 vcc, exec, s[26:27]
	s_cbranch_vccnz .Lu2_7
	s_waitcnt lgkmcnt(0)
	v_add_u32_e32 v98, s38, v212
	ds_read_b128 v[86:89], v98 offset:49248
	ds_read_b128 v[90:93], v98 offset:49216
	ds_read_b128 v[94:97], v98 offset:49152
	ds_read_b128 v[98:101], v98 offset:49184
	s_waitcnt lgkmcnt(3)
	v_pk_mul_f32 v[16:17], v[16:17], v[88:89]
	v_pk_mul_f32 v[14:15], v[14:15], v[86:87]
	s_waitcnt lgkmcnt(2)
	v_pk_mul_f32 v[12:13], v[12:13], v[92:93]
	v_pk_mul_f32 v[10:11], v[10:11], v[90:91]
	s_waitcnt lgkmcnt(0)
	v_pk_mul_f32 v[8:9], v[8:9], v[100:101]
	v_pk_mul_f32 v[6:7], v[6:7], v[98:99]
	v_pk_mul_f32 v[4:5], v[4:5], v[96:97]
	v_pk_mul_f32 v[2:3], v[2:3], v[94:95]
	v_pk_mul_f32 v[32:33], v[32:33], v[88:89]
	v_pk_mul_f32 v[30:31], v[30:31], v[86:87]
	v_pk_mul_f32 v[28:29], v[28:29], v[92:93]
	v_pk_mul_f32 v[26:27], v[26:27], v[90:91]
	v_pk_mul_f32 v[24:25], v[24:25], v[100:101]
	v_pk_mul_f32 v[22:23], v[22:23], v[98:99]
	v_pk_mul_f32 v[20:21], v[20:21], v[96:97]
	v_pk_mul_f32 v[18:19], v[18:19], v[94:95]
